# speedup vs baseline: 1.0332x; 1.0002x over previous
.Ltg0_go:
	s_nop 1
	v_accvgpr_read_b32 v10, a128
	v_accvgpr_read_b32 v11, a129
	v_accvgpr_read_b32 v12, a130
	v_accvgpr_read_b32 v13, a131
	v_cvt_pk_f16_f32 v1, v12, v13
	v_cvt_pk_f16_f32 v0, v10, v11
	v_accvgpr_read_b32 v6, a132
	v_accvgpr_read_b32 v7, a133
	v_accvgpr_read_b32 v8, a134
	v_accvgpr_read_b32 v9, a135
	v_cvt_pk_f16_f32 v3, v8, v9
	v_cvt_pk_f16_f32 v2, v6, v7
	ds_write2_b64 v221, v[0:1], v[2:3] offset0:48 offset1:80
	s_cmp_lt_u32 s25, 12
	s_cbranch_scc0 .Lmd_dec
	s_and_saveexec_b64 s[36:37], s[6:7]
	v_add_u32_e32 v0, 0x8400, v60
	s_waitcnt vmcnt(0)
	ds_write2_b32 v0, v181, v184 offset1:16
	ds_write_b32 v60, v185 offset:33920
	s_mov_b64 exec, s[36:37]
	s_waitcnt lgkmcnt(0)
	s_barrier
.LBB1_106:
	v_add_u32_e32 v184, v110, v224
	ds_read_b128 v[6:9], v225 offset:33792
	ds_read_b128 v[10:13], v225 offset:33856
	v_add_u32_e32 v250, v110, v226
	v_add_u32_e32 v185, v110, v227
	ds_read_b32 v20, v184 offset:21504
	ds_read_b32 v21, v250 offset:21504
	ds_read_b32 v22, v185 offset:21504
	ds_read_b128 v[14:17], v225 offset:33920
	v_add_u32_e32 v251, v110, v228
	ds_read_b32 v23, v251 offset:21504
	s_waitcnt lgkmcnt(6)
	v_mov_b32_e32 v0, v6
	s_waitcnt lgkmcnt(5)
	v_mov_b32_e32 v1, v10
	s_waitcnt vmcnt(5)
	v_mul_f32_e32 v2, v182, v6
	s_waitcnt vmcnt(4)
	v_pk_fma_f32 v[0:1], v[182:183], v[0:1], v[2:3] op_sel_hi:[1,1,0]
	s_waitcnt vmcnt(0) lgkmcnt(1)
	v_mul_f32_e32 v181, v186, v14
	v_accvgpr_read_b32 v0, a4
	v_pk_add_f32 v[0:1], v[180:181], v[0:1]
	v_mul_f32_e32 v2, v182, v7
	v_add_f32_e32 v0, v0, v1
	v_mul_f32_e32 v0, 0xbfb8aa3b, v0
	v_exp_f32_e32 v3, v0
	v_mov_b32_e32 v0, v7
	v_mov_b32_e32 v1, v11
	v_mul_f32_e32 v181, v186, v15
	v_pk_fma_f32 v[0:1], v[182:183], v[0:1], v[2:3] op_sel_hi:[1,1,0]
	v_mul_f32_e32 v2, v182, v8
	v_accvgpr_read_b32 v0, a5
	v_pk_add_f32 v[0:1], v[180:181], v[0:1]
	v_mul_f32_e32 v181, v186, v16
	v_add_f32_e32 v0, v0, v1
	v_mul_f32_e32 v0, 0xbfb8aa3b, v0
	v_exp_f32_e32 v0, v0
	v_add_f32_e32 v1, 1.0, v3
	v_rcp_f32_e32 v24, v1
	v_mov_b32_e32 v1, v12
	v_add_f32_e32 v3, 1.0, v0
	v_mov_b32_e32 v0, v8
	v_pk_fma_f32 v[0:1], v[182:183], v[0:1], v[2:3] op_sel_hi:[1,1,0]
	v_mul_f32_e32 v2, v182, v9
	v_accvgpr_read_b32 v0, a6
	v_pk_add_f32 v[0:1], v[180:181], v[0:1]
	v_mul_f32_e32 v181, v186, v17
	v_add_f32_e32 v0, v0, v1
	v_mul_f32_e32 v0, 0xbfb8aa3b, v0
	v_exp_f32_e32 v18, v0
	v_mov_b32_e32 v0, v9
	v_mov_b32_e32 v1, v13
	v_pk_fma_f32 v[0:1], v[182:183], v[0:1], v[2:3] op_sel_hi:[1,1,0]
	v_rcp_f32_e32 v25, v3
	v_accvgpr_read_b32 v0, a7
	v_pk_add_f32 v[0:1], v[180:181], v[0:1]
	s_andn2_b64 vcc, exec, s[28:29]
	s_mov_b64 s[16:17], vcc
	v_add_f32_e32 v0, v0, v1
	v_mul_f32_e32 v0, 0xbfb8aa3b, v0
	v_exp_f32_e32 v0, v0
	v_add_f32_e32 v1, 1.0, v18
	v_rcp_f32_e32 v26, v1
	v_mul_f32_e32 v1, v21, v25
	v_add_f32_e32 v0, 1.0, v0
	v_rcp_f32_e32 v27, v0
	v_mul_f32_e32 v2, v22, v26
	v_mul_f32_e32 v0, v20, v24
	v_cvt_pk_f16_f32 v18, v0, v1
	s_waitcnt lgkmcnt(0)
	v_mul_f32_e32 v3, v23, v27
	v_cvt_pk_f16_f32 v19, v2, v3
	v_or_b32_e32 v19, s64, v19
	s_cbranch_vccnz .LBB1_171
	global_store_dwordx2 v[172:173], v[18:19], off
	s_or_b32 s70, s40, 1
	s_and_saveexec_b64 s[68:69], s[12:13]
	v_mov_b32_e32 v3, s70
	global_store_dword v[174:175], v3, off
	s_mov_b64 exec, s[68:69]
	s_cbranch_execnz .LBB1_109

.Ltg1_go:
	s_nop 1
	v_accvgpr_read_b32 v0, a0
	v_accvgpr_read_b32 v2, a1
	v_accvgpr_read_b32 v1, a2
	v_accvgpr_read_b32 v3, a3
	v_cvt_pk_f16_f32 v1, v1, v3
	v_cvt_pk_f16_f32 v0, v0, v2
	v_add_u32_e32 v182, v111, v207
	v_accvgpr_read_b32 v2, a4
	v_accvgpr_read_b32 v6, a5
	v_accvgpr_read_b32 v3, a6
	v_accvgpr_read_b32 v7, a7
	v_cvt_pk_f16_f32 v3, v3, v7
	v_cvt_pk_f16_f32 v2, v2, v6
	ds_write2_b64 v248, v[0:1], v[2:3] offset0:80 offset1:96
	s_waitcnt lgkmcnt(0)
	s_barrier
	ds_read_b128 v[0:3], v182 offset:12800
	ds_read_b128 v[6:9], v182 offset:12864
	ds_read_b128 v[10:13], v182 offset:12928
	ds_read_b128 v[14:17], v182 offset:12992
	ds_read_b128 v[18:21], v182 offset:13056
	ds_read_b128 v[22:25], v182 offset:13120
	ds_read2st64_b32 v[42:43], v242 offset0:84 offset1:116
	ds_read_b128 v[38:41], v225 offset:33792
	ds_read_b128 v[26:29], v225 offset:33856
	ds_read_b128 v[30:33], v225 offset:33920
	v_or_b32_e32 v36, v110, v227
	v_or_b32_e32 v34, v110, v226
	ds_read2st64_b32 v[44:45], v36 offset0:84 offset1:116
	v_or_b32_e32 v36, v110, v228
	ds_read2st64_b32 v[34:35], v34 offset0:84 offset1:116
	ds_read2st64_b32 v[36:37], v36 offset0:84 offset1:116
	s_waitcnt lgkmcnt(12)
	v_mfma_f32_16x16x32_f16 a[0:3], v[0:3], a[56:59], 0
	s_waitcnt lgkmcnt(11)
	v_mfma_f32_16x16x32_f16 a[0:3], v[6:9], a[60:63], a[0:3]
	s_waitcnt lgkmcnt(10)
	v_mfma_f32_16x16x32_f16 a[0:3], v[10:13], a[64:67], a[0:3]
	s_waitcnt lgkmcnt(9)
	v_mfma_f32_16x16x32_f16 a[0:3], v[14:17], a[68:71], a[0:3]
	s_waitcnt lgkmcnt(8)
	v_mfma_f32_16x16x32_f16 a[0:3], v[18:21], a[72:75], a[0:3]
	s_waitcnt lgkmcnt(7)
	v_mfma_f32_16x16x32_f16 a[0:3], v[22:25], a[76:79], a[0:3]
	s_waitcnt vmcnt(0) lgkmcnt(3)
	v_mul_f32_e32 v0, v191, v26
	v_mul_f32_e32 v1, v191, v27
	v_mul_f32_e32 v2, v191, v28
	v_mul_f32_e32 v3, v191, v29
	v_fma_f32 v0, v190, v38, v0
	v_fma_f32 v1, v190, v39, v1
	v_fma_f32 v2, v190, v40, v2
	v_fma_f32 v3, v190, v41, v3
	v_mul_f32_e32 v6, v192, v30
	v_mul_f32_e32 v7, v192, v31
	v_mul_f32_e32 v8, v192, v32
	v_mul_f32_e32 v9, v192, v33
	v_add_f32_e32 v46, v0, v6
	v_add_f32_e32 v47, v1, v7
	v_add_f32_e32 v48, v2, v8
	v_add_f32_e32 v49, v3, v9
	v_accvgpr_read_b32 v0, a0
	v_accvgpr_read_b32 v1, a1
	v_accvgpr_read_b32 v2, a2
	v_accvgpr_read_b32 v3, a3
	v_add_f32_e32 v0, v186, v0
	v_add_f32_e32 v1, v186, v1
	v_add_f32_e32 v2, v186, v2
	v_add_f32_e32 v3, v186, v3
	v_add_f32_e32 v0, v46, v0
	v_add_f32_e32 v1, v47, v1
	v_add_f32_e32 v2, v48, v2
	v_add_f32_e32 v3, v49, v3
	v_mul_f32_e32 v0, 0x4038aa3b, v0
	v_mul_f32_e32 v1, 0x4038aa3b, v1
	v_mul_f32_e32 v2, 0x4038aa3b, v2
	v_mul_f32_e32 v3, 0x4038aa3b, v3
	v_exp_f32_e32 v0, v0
	v_exp_f32_e32 v1, v1
	v_exp_f32_e32 v2, v2
	v_exp_f32_e32 v3, v3
	v_add_f32_e32 v0, 1.0, v0
	v_add_f32_e32 v1, 1.0, v1
	v_add_f32_e32 v2, 1.0, v2
	v_add_f32_e32 v3, 1.0, v3
	v_rcp_f32_e32 v0, v0
	v_rcp_f32_e32 v1, v1
	v_rcp_f32_e32 v2, v2
	v_rcp_f32_e32 v3, v3
	s_waitcnt lgkmcnt(0)
	s_and_b64 vcc, exec, s[16:17]
	v_sub_f32_e32 v6, 1.0, v43
	v_sub_f32_e32 v7, 1.0, v35
	v_sub_f32_e32 v12, 1.0, v45
	v_sub_f32_e32 v13, 1.0, v37
	v_fma_f32 v0, -v0, 2.0, 1.0
	v_fma_f32 v1, -v1, 2.0, 1.0
	v_fma_f32 v2, -v2, 2.0, 1.0
	v_fma_f32 v3, -v3, 2.0, 1.0
	v_mul_f32_e32 v0, v6, v0
	v_mul_f32_e32 v1, v7, v1
	v_mul_f32_e32 v2, v12, v2
	v_mul_f32_e32 v3, v13, v3
	v_fma_f32 v8, v42, v43, v0
	v_fma_f32 v9, v34, v35, v1
	v_fma_f32 v10, v44, v45, v2
	v_fma_f32 v11, v36, v37, v3
	v_cvt_pk_f16_f32 v6, v8, v9
	v_cvt_pk_f16_f32 v7, v10, v11
	v_mov_b32_e32 v2, v6
	v_or_b32_e32 v3, s64, v7
	s_cbranch_vccnz .LBB1_125
	global_store_dwordx2 v[178:179], v[2:3], off
	s_or_b32 s70, s40, 2
	s_and_saveexec_b64 s[68:69], s[12:13]
	v_mov_b32_e32 v0, s70
	global_store_dword v[174:175], v0, off
	s_mov_b64 exec, s[68:69]
	s_mov_b64 s[36:37], 0

.Ltg2_go:
	s_nop 1
	v_accvgpr_read_b32 v30, a128
	v_accvgpr_read_b32 v32, a129
	v_accvgpr_read_b32 v31, a130
	v_accvgpr_read_b32 v33, a131
	v_cvt_pk_f16_f32 v31, v31, v33
	v_cvt_pk_f16_f32 v30, v30, v32
	v_accvgpr_read_b32 v32, a132
	v_accvgpr_read_b32 v34, a133
	v_accvgpr_read_b32 v33, a134
	v_accvgpr_read_b32 v35, a135
	v_cvt_pk_f16_f32 v33, v33, v35
	v_cvt_pk_f16_f32 v32, v32, v34
	ds_write2_b64 v221, v[30:31], v[32:33] offset0:32 offset1:64
	s_waitcnt lgkmcnt(0)
	s_barrier
	ds_read_b128 v[34:37], v249
	ds_read_b128 v[38:41], v249 offset:64
	ds_read_b128 v[42:45], v249 offset:256
	ds_read_b128 v[46:49], v249 offset:320
	ds_read_b128 v[50:53], v249 offset:512
	ds_read_b128 v[30:33], v249 offset:576
	ds_read2st64_b32 v[56:57], v184 offset0:100 offset1:101
	ds_read2st64_b32 v[54:55], v184 offset0:102 offset1:103
	s_waitcnt lgkmcnt(7)
	v_mfma_f32_16x16x32_f16 a[4:7], v[34:37], v[0:3], a[4:7]
	s_waitcnt lgkmcnt(6)
	v_mfma_f32_16x16x32_f16 a[4:7], v[38:41], v[64:67], a[4:7]
	s_waitcnt lgkmcnt(5)
	v_mfma_f32_16x16x32_f16 a[4:7], v[42:45], v[68:71], a[4:7]
	s_waitcnt lgkmcnt(4)
	v_mfma_f32_16x16x32_f16 a[4:7], v[46:49], v[72:75], a[4:7]
	s_waitcnt lgkmcnt(3)
	v_mfma_f32_16x16x32_f16 a[4:7], v[50:53], v[78:81], a[4:7]
	s_waitcnt lgkmcnt(2)
	v_mfma_f32_16x16x32_f16 a[4:7], v[30:33], v[82:85], a[4:7]
	s_nop 7
	v_accvgpr_read_b32 v0, a4
	s_waitcnt vmcnt(0)
	v_add_f32_e32 v0, v180, v0
	v_accvgpr_read_b32 v1, a5
	v_mul_f32_e32 v0, 0xbfb8aa3b, v0
	v_add_f32_e32 v1, v180, v1
	v_exp_f32_e32 v0, v0
	v_mul_f32_e32 v1, 0xbfb8aa3b, v1
	v_exp_f32_e32 v1, v1
	v_accvgpr_read_b32 v2, a7
	v_add_f32_e32 v0, 1.0, v0
	v_rcp_f32_e32 v186, v0
	v_add_f32_e32 v0, 1.0, v1
	v_accvgpr_read_b32 v1, a6
	v_add_f32_e32 v1, v180, v1
	v_mul_f32_e32 v1, 0xbfb8aa3b, v1
	v_add_f32_e32 v2, v180, v2
	v_exp_f32_e32 v1, v1
	v_mul_f32_e32 v2, 0xbfb8aa3b, v2
	v_exp_f32_e32 v2, v2
	v_rcp_f32_e32 v252, v0
	v_add_f32_e32 v0, 1.0, v1
	v_rcp_f32_e32 v253, v0
	v_add_f32_e32 v0, 1.0, v2
	v_rcp_f32_e32 v254, v0
	s_waitcnt lgkmcnt(1)
	v_mul_f32_e32 v0, v56, v186
	v_mul_f32_e32 v1, v57, v252
	s_waitcnt lgkmcnt(0)
	v_mul_f32_e32 v2, v54, v253
	v_mul_f32_e32 v3, v55, v254
	v_cvt_pk_f16_f32 v181, v2, v3
	s_and_b64 vcc, exec, s[16:17]
	v_cvt_pk_f16_f32 v180, v0, v1
	s_cbranch_vccnz .LBB1_143
	global_store_dwordx2 v[172:173], v[180:181], off
	s_or_b32 s70, s40, 3
	s_and_saveexec_b64 s[68:69], s[12:13]
	v_mov_b32_e32 v3, s70
	global_store_dword v[174:175], v3, off
	s_mov_b64 exec, s[68:69]
	s_mov_b64 s[36:37], 0

.Lmd_dec:
	s_cmp_eq_u32 s25, 12
	s_cbranch_scc0 .Lmd_m2
	s_and_saveexec_b64 s[36:37], s[8:9]
	ds_write_b32 v60, v59 offset:33792
	s_mov_b64 exec, s[36:37]
	s_waitcnt lgkmcnt(0)
	s_barrier
	s_branch .LBB1_106
.Lmd_m2:
	v_accvgpr_read_b32 v14, a138
	v_accvgpr_read_b32 v15, a139
	v_fma_f32 v0, v14, v10, 0
	v_accvgpr_read_b32 v16, a140
	v_fmac_f32_e32 v0, v15, v11
	v_accvgpr_read_b32 v17, a141
	v_fmac_f32_e32 v0, v16, v12
	v_fmac_f32_e32 v0, v17, v13
	v_fma_f32 v10, v14, v6, 0
	v_fmac_f32_e32 v10, v15, v7
	v_fmac_f32_e32 v10, v16, v8
	v_fmac_f32_e32 v10, v17, v9
	v_mov_b32_e32 v3, v0
	v_mov_b32_e32 v1, v10
	s_nop 1
	v_permlane16_swap_b32_e32 v0, v3
	v_permlane16_swap_b32_e32 v10, v1
	v_add_f32_e32 v6, v0, v3
	v_add_f32_e32 v8, v10, v1
	v_mov_b32_e32 v7, v6
	v_mov_b32_e32 v9, v8
	s_nop 1
	v_permlane32_swap_b32_e32 v6, v7
	v_permlane32_swap_b32_e32 v8, v9
	s_and_saveexec_b64 s[36:37], s[10:11]
	s_cbranch_execz .LBB1_101
	v_accvgpr_read_b32 v2, a144
	v_accvgpr_read_b32 v3, a145
	v_add_u32_e32 v2, v2, v3
	s_waitcnt lgkmcnt(0)
	v_add_f32_e32 v0, v8, v9
	v_add_f32_e32 v1, v6, v7
	v_add_u32_e32 v2, 0x8400, v2
	ds_write2_b32 v2, v1, v0 offset0:64 offset1:80
.LBB1_101:
	s_or_b64 exec, exec, s[36:37]
	s_waitcnt lgkmcnt(0)
	s_barrier
	s_and_saveexec_b64 s[16:17], s[2:3]
	s_cbranch_execz .LBB1_105
	v_add_u32_e32 v2, 0x8400, v60
	ds_read2_b32 v[0:1], v2 offset0:64 offset1:96
	ds_read2_b32 v[6:7], v2 offset0:128 offset1:160
	s_waitcnt lgkmcnt(1)
	v_add_f32_e32 v3, v0, v1
	s_waitcnt lgkmcnt(0)
	v_add_f32_e32 v0, v3, v6
	v_add_f32_e32 v0, v0, v7
	v_accvgpr_read_b32 v1, a238
	v_add_f32_e32 v0, v1, v0
	v_accvgpr_read_b32 v1, a239
	ds_write_b32 v1, v0 offset:33856
.LBB1_105:
	s_or_b64 exec, exec, s[16:17]
	s_waitcnt lgkmcnt(0)
	s_barrier
	s_branch .LBB1_106
